# speedup vs baseline: 1.0327x; 1.0149x over previous
.LBB6_6:
	v_lshlrev_b32_e32 v30, 3, v22
	v_or_b32_e32 v22, s18, v28
	v_mov_b32_e32 v23, s19
	v_lshlrev_b64 v[22:23], 13, v[22:23]
	v_lshl_add_u64 v[80:81], s[14:15], 0, v[22:23]
	v_lshrrev_b32_e32 v104, 2, v203
	v_lshlrev_b32_e32 v22, 1, v204
	v_bfe_u32 v23, v203, 2, 2
	s_and_b32 s7, s33, 3
	s_lshl_b32 s7, s7, 13
	s_lshr_b32 s62, s33, 2
	s_lshl_b32 s62, s62, 17
	s_mov_b32 s63, 0
	s_lshr_b32 s64, s33, 2
	s_lshl_b32 s64, s64, 12
	s_add_i32 s65, s64, 0x8000
	v_bitop3_b32 v24, v22, v104, 3 bitop3:0x78
	v_bitop3_b32 v22, v22, v23, 1 bitop3:0x36
	s_cmp_lg_u32 0, -1
	v_lshlrev_b32_e32 v218, 4, v22
	v_bitop3_b32 v22, v28, v0, 15 bitop3:0x78
	s_cselect_b32 s0, 0, 0
	v_lshlrev_b32_e32 v26, 4, v22
	s_add_i32 s41, s0, s7
	v_lshl_add_u64 v[164:165], v[80:81], 0, v[26:27]
	s_mov_b64 s[0:1], 0x0
	v_and_b32_e32 v31, 15, v0
	v_lshl_add_u64 v[22:23], v[164:165], 0, s[0:1]
	v_lshl_add_u64 v[22:23], v[22:23], 0, s[62:63]
	s_add_i32 s38, s41, 0x14800
	s_add_i32 m0, s38, s64
	s_nop 0
	global_load_lds_dwordx4 v[22:23], off nt
	v_bitop3_b32 v22, v28, v31, 4 bitop3:0x36
	v_lshlrev_b32_e32 v26, 4, v22
	v_lshl_add_u64 v[22:23], v[80:81], 0, v[26:27]
	s_mov_b64 s[8:9], 0x8000
	v_lshlrev_b32_e32 v217, 4, v24
	v_lshl_add_u64 v[24:25], v[22:23], 0, s[8:9]
	v_lshl_add_u64 v[24:25], v[24:25], 0, s[62:63]
	s_add_i32 s8, s41, 0x14c00
	s_add_i32 m0, s8, s64
	s_nop 0
	global_load_lds_dwordx4 v[24:25], off nt
	v_bitop3_b32 v24, v28, v31, 8 bitop3:0x36
	v_lshlrev_b32_e32 v26, 4, v24
	v_lshl_add_u64 v[24:25], v[80:81], 0, v[26:27]
	s_mov_b64 s[8:9], 0x10000
	v_bitop3_b32 v26, v28, v31, 12 bitop3:0x36
	v_lshl_add_u64 v[82:83], v[24:25], 0, s[8:9]
	v_lshl_add_u64 v[82:83], v[82:83], 0, s[62:63]
	s_add_i32 s8, s41, 0x15000
	s_add_i32 m0, s8, s64
	s_nop 0
	global_load_lds_dwordx4 v[82:83], off nt
	v_lshlrev_b32_e32 v26, 4, v26
	v_lshl_add_u64 v[26:27], v[80:81], 0, v[26:27]
	s_mov_b64 s[8:9], 0x18000
	v_lshl_add_u64 v[80:81], v[26:27], 0, s[8:9]
	v_lshl_add_u64 v[80:81], v[80:81], 0, s[62:63]
	s_add_i32 s8, s41, 0x15400
	s_add_i32 m0, s8, s64
	s_nop 0
	global_load_lds_dwordx4 v[80:81], off nt
	s_mov_b64 s[14:15], 0x20000
	s_add_i32 s14, s41, 0x15800
	s_mov_b64 s[14:15], 0x28000
	s_add_i32 s14, s41, 0x15c00
	s_mov_b64 s[34:35], 0x30000
	s_add_i32 s34, s41, 0x16000
	s_mov_b64 s[34:35], 0x38000
	v_lshl_add_u32 v216, v203, 6, 0
	v_add_u32_e32 v216, s57, v216
	s_add_i32 s41, s41, 0x16400
	s_waitcnt vmcnt(0) lgkmcnt(0)
	s_barrier
	v_and_b32_e32 v226, 31, v0
	v_bfe_u32 v227, v0, 5, 1
	v_lshrrev_b32_e32 v228, 2, v226
	v_lshlrev_b32_e32 v228, 10, v228
	v_and_b32_e32 v229, 3, v226
	v_lshlrev_b32_e32 v229, 8, v229
	v_add3_u32 v230, s38, v228, v229
	v_and_b32_e32 v231, 15, v226
	v_xor_b32_e32 v231, v231, v227
	v_lshlrev_b32_e32 v231, 4, v231
	v_mov_b32_e32 v232, v231
	v_add_u32_e32 v232, v230, v232
	ds_read_b128 v[64:67], v232
	v_xor_b32_e32 v233, 0x80, v231
	v_add_u32_e32 v233, v230, v233
	ds_read_b128 v[2:5], v233
	v_xor_b32_e32 v234, 0x20, v231
	v_add_u32_e32 v234, v230, v234
	ds_read_b128 v[68:71], v234
	v_xor_b32_e32 v235, 0xa0, v231
	v_add_u32_e32 v235, v230, v235
	ds_read_b128 v[6:9], v235
	v_xor_b32_e32 v236, 0x40, v231
	v_add_u32_e32 v236, v230, v236
	ds_read_b128 v[72:75], v236
	v_xor_b32_e32 v237, 0xc0, v231
	v_add_u32_e32 v237, v230, v237
	ds_read_b128 v[10:13], v237
	v_xor_b32_e32 v238, 0x60, v231
	v_add_u32_e32 v238, v230, v238
	ds_read_b128 v[76:79], v238
	v_xor_b32_e32 v239, 0xe0, v231
	v_add_u32_e32 v239, v230, v239
	ds_read_b128 v[14:17], v239
	s_waitcnt lgkmcnt(0)
	s_mov_b64 s[52:53], 0x100
	v_lshl_add_u64 v[224:225], v[164:165], 0, s[52:53]
	v_lshl_add_u64 v[224:225], v[224:225], 0, s[62:63]
	s_add_i32 s54, s38, 0x0
	s_add_i32 m0, s54, s65
	s_nop 0
	global_load_lds_dwordx4 v[224:225], off nt
	s_mov_b64 s[52:53], 0x8100
	v_lshl_add_u64 v[224:225], v[22:23], 0, s[52:53]
	v_lshl_add_u64 v[224:225], v[224:225], 0, s[62:63]
	s_add_i32 s54, s38, 0x400
	s_add_i32 m0, s54, s65
	s_nop 0
	global_load_lds_dwordx4 v[224:225], off nt
	s_mov_b64 s[52:53], 0x10100
	v_lshl_add_u64 v[224:225], v[24:25], 0, s[52:53]
	v_lshl_add_u64 v[224:225], v[224:225], 0, s[62:63]
	s_add_i32 s54, s38, 0x800
	s_add_i32 m0, s54, s65
	s_nop 0
	global_load_lds_dwordx4 v[224:225], off nt
	s_mov_b64 s[52:53], 0x18100
	v_lshl_add_u64 v[224:225], v[26:27], 0, s[52:53]
	v_lshl_add_u64 v[224:225], v[224:225], 0, s[62:63]
	s_add_i32 s54, s38, 0xc00
	s_add_i32 m0, s54, s65
	s_nop 0
	global_load_lds_dwordx4 v[224:225], off nt
	s_mov_b64 s[52:53], 0x20100
	s_add_i32 s54, s38, 0x1000
	s_mov_b64 s[52:53], 0x28100
	s_add_i32 s54, s38, 0x1400
	s_mov_b64 s[52:53], 0x30100
	s_add_i32 s54, s38, 0x1800
	s_mov_b64 s[52:53], 0x38100
	s_add_i32 s54, s38, 0x1c00
	v_add_u32_e32 v209, v216, v217
	v_add_u32_e32 v210, v216, v218
	ds_read_b128 v[80:83], v209
	ds_read_b128 v[88:91], v209 offset:2048
	ds_read_b128 v[84:87], v210
	ds_read_b128 v[92:95], v210 offset:2048
	v_mov_b32_e32 v219, 0x7f7f7f7f
	v_mov_b32_e32 v220, 0x7c7c7c7c
	s_waitcnt vmcnt(10) lgkmcnt(1)
	v_mfma_scale_f32_32x32x64_f8f6f4 v[64:79], v[80:87], v[96:103], v[64:79], v219, v220 op_sel_hi:[0,0,0]
	s_waitcnt vmcnt(8) lgkmcnt(0)
	v_mfma_scale_f32_32x32x64_f8f6f4 v[2:17], v[88:95], v[96:103], v[2:17], v219, v220 op_sel_hi:[0,0,0]
	s_mov_b32 s41, 0x3fb8aa3b
	s_nop 15
	s_nop 15
	s_nop 15
	s_nop 15
	s_nop 15
	s_nop 15
	s_waitcnt vmcnt(0) lgkmcnt(0)
	s_barrier
	ds_read_b128 v[48:51], v232 offset:32768
	ds_read_b128 v[32:35], v233 offset:32768
	ds_read_b128 v[52:55], v234 offset:32768
	ds_read_b128 v[36:39], v235 offset:32768
	ds_read_b128 v[56:59], v236 offset:32768
	ds_read_b128 v[40:43], v237 offset:32768
	ds_read_b128 v[60:63], v238 offset:32768
	ds_read_b128 v[44:47], v239 offset:32768
	s_waitcnt lgkmcnt(0)
	s_mov_b64 s[52:53], 0x200
	v_lshl_add_u64 v[224:225], v[164:165], 0, s[52:53]
	v_lshl_add_u64 v[224:225], v[224:225], 0, s[62:63]
	s_add_i32 s54, s38, 0x0
	s_add_i32 m0, s54, s64
	s_nop 0
	global_load_lds_dwordx4 v[224:225], off nt
	s_mov_b64 s[52:53], 0x8200
	v_lshl_add_u64 v[224:225], v[22:23], 0, s[52:53]
	v_lshl_add_u64 v[224:225], v[224:225], 0, s[62:63]
	s_add_i32 s54, s38, 0x400
	s_add_i32 m0, s54, s64
	s_nop 0
	global_load_lds_dwordx4 v[224:225], off nt
	s_mov_b64 s[52:53], 0x10200
	v_lshl_add_u64 v[224:225], v[24:25], 0, s[52:53]
	v_lshl_add_u64 v[224:225], v[224:225], 0, s[62:63]
	s_add_i32 s54, s38, 0x800
	s_add_i32 m0, s54, s64
	s_nop 0
	global_load_lds_dwordx4 v[224:225], off nt
	s_mov_b64 s[52:53], 0x18200
	v_lshl_add_u64 v[224:225], v[26:27], 0, s[52:53]
	v_lshl_add_u64 v[224:225], v[224:225], 0, s[62:63]
	s_add_i32 s54, s38, 0xc00
	s_add_i32 m0, s54, s64
	s_nop 0
	global_load_lds_dwordx4 v[224:225], off nt
	v_lshlrev_b32_e32 v29, 2, v204
	v_max_f32_e32 v80, v65, v65
	v_max_f32_e32 v81, v64, v64
	v_max_f32_e32 v80, v81, v80
	v_max3_f32 v81, v66, v67, v3
	v_max3_f32 v80, v80, v2, v4
	v_max3_f32 v80, v80, v5, v68
	v_max3_f32 v81, v81, v70, v71
	v_max3_f32 v80, v80, v69, v6
	v_max3_f32 v81, v81, v8, v9
	v_max3_f32 v80, v80, v7, v72
	v_max3_f32 v81, v81, v74, v75
	v_max3_f32 v80, v80, v73, v10
	v_max3_f32 v81, v81, v12, v13
	v_max3_f32 v80, v80, v11, v76
	v_max3_f32 v81, v81, v78, v79
	v_max3_f32 v80, v80, v77, v14
	v_max3_f32 v81, v81, v16, v17
	v_max3_f32 v80, v80, v15, v81
	v_mov_b32_e32 v81, v80
	s_nop 1
	v_permlane32_swap_b32_e32 v80, v81
	v_max_f32_e32 v81, v81, v81
	v_max_f32_e32 v80, v80, v80
	v_max_f32_e32 v80, v80, v81
	v_mul_f32_e32 v208, 0x3fb8aa3b, v80
	s_mov_b32 s27, 0
	s_mov_b32 s40, -1
	s_mov_b64 s[0:1], 0x8000
	s_mov_b64 s[28:29], 0x10000
	s_mov_b64 s[20:21], 0x18000
	s_mov_b64 s[8:9], 0x20000
	s_mov_b64 s[30:31], 0x28000
	s_mov_b64 s[14:15], 0x30000
	s_mov_b64 s[34:35], 0x38000
	v_fma_f32 v64, v64, s41, -v208
	v_fma_f32 v2, v2, s41, -v208
	v_fma_f32 v65, v65, s41, -v208
	v_fma_f32 v3, v3, s41, -v208
	v_fma_f32 v66, v66, s41, -v208
	v_fma_f32 v4, v4, s41, -v208
	v_fma_f32 v67, v67, s41, -v208
	v_fma_f32 v5, v5, s41, -v208
	v_fma_f32 v68, v68, s41, -v208
	v_fma_f32 v6, v6, s41, -v208
	v_fma_f32 v69, v69, s41, -v208
	v_fma_f32 v7, v7, s41, -v208
	v_fma_f32 v70, v70, s41, -v208
	v_fma_f32 v8, v8, s41, -v208
	v_fma_f32 v71, v71, s41, -v208
	v_fma_f32 v9, v9, s41, -v208
	v_fma_f32 v72, v72, s41, -v208
	v_fma_f32 v10, v10, s41, -v208
	v_fma_f32 v73, v73, s41, -v208
	v_fma_f32 v11, v11, s41, -v208
	v_fma_f32 v74, v74, s41, -v208
	v_fma_f32 v12, v12, s41, -v208
	v_fma_f32 v75, v75, s41, -v208
	v_fma_f32 v13, v13, s41, -v208
	v_fma_f32 v76, v76, s41, -v208
	v_fma_f32 v14, v14, s41, -v208
	v_fma_f32 v77, v77, s41, -v208
	v_fma_f32 v78, v78, s41, -v208
	v_fma_f32 v79, v79, s41, -v208
	v_fma_f32 v94, v15, s41, -v208
	v_fma_f32 v16, v16, s41, -v208
	v_fma_f32 v15, v17, s41, -v208
	s_and_b64 vcc, exec, s[4:5]
	s_nop 0
	v_lshl_add_u64 v[20:21], v[20:21], 0, s[14:15]
	s_mov_b32 m0, s39
	s_nop 0
	global_load_lds_dwordx4 v[20:21], off

.LBB6_9:
	v_add_u32_e32 v138, s27, v207
	ds_read_b64_tr_b16 v[156:157], v138 offset:24576
	ds_read_b64_tr_b16 v[158:159], v138 offset:25088
	v_add_f32_e32 v120, v80, v81
	s_waitcnt lgkmcnt(3)
	v_mfma_scale_f32_32x32x64_f8f6f4 v[48:63], v[112:119], v[96:103], v[48:63], v219, v220 op_sel_hi:[0,0,0]
	v_add_f32_e32 v112, v82, v120
	v_add_f32_e32 v112, v83, v112
	v_add_f32_e32 v112, v84, v112
	v_add_f32_e32 v116, v85, v112
	v_cvt_pk_f16_f32 v132, v80, v81
	v_cvt_pk_f16_f32 v133, v82, v83
	ds_read_b64_tr_b16 v[112:113], v138 offset:28672
	ds_read_b64_tr_b16 v[114:115], v138 offset:29184
	v_add_f32_e32 v80, v86, v116
	v_add_f32_e32 v80, v87, v80
	v_add_f32_e32 v80, v88, v80
	v_add_f32_e32 v80, v89, v80
	v_cvt_pk_f16_f32 v134, v84, v85
	v_cvt_pk_f16_f32 v135, v86, v87
	s_waitcnt lgkmcnt(4)
	v_mfma_scale_f32_32x32x64_f8f6f4 v[32:47], v[104:111], v[96:103], v[32:47], v219, v220 op_sel_hi:[0,0,0]
	v_lshl_add_u64 v[186:187], v[164:165], 0, s[2:3]
	v_lshl_add_u64 v[228:229], v[186:187], 0, s[10:11]
	v_lshl_add_u64 v[228:229], v[228:229], 0, s[62:63]
	s_add_i32 m0, s38, s65
	s_nop 0
	global_load_lds_dwordx4 v[228:229], off nt
	ds_read_b64_tr_b16 v[104:105], v138 offset:25600
	ds_read_b64_tr_b16 v[106:107], v138 offset:26112
	v_lshl_add_u64 v[188:189], v[178:179], 0, s[2:3]
	v_lshl_add_u64 v[228:229], v[188:189], 0, s[10:11]
	v_lshl_add_u64 v[228:229], v[228:229], 0, s[62:63]
	s_add_i32 m0, s30, s65
	s_nop 0
	global_load_lds_dwordx4 v[228:229], off nt
	v_add_f32_e32 v80, v90, v80
	v_add_f32_e32 v80, v91, v80
	v_add_f32_e32 v80, v92, v80
	v_add_f32_e32 v80, v93, v80
	v_cvt_pk_f16_f32 v128, v88, v89
	v_cvt_pk_f16_f32 v129, v90, v91
	ds_read_b64_tr_b16 v[152:153], v138 offset:29696
	ds_read_b64_tr_b16 v[154:155], v138 offset:30208
	v_lshl_add_u64 v[190:191], v[176:177], 0, s[2:3]
	v_lshl_add_u64 v[228:229], v[190:191], 0, s[10:11]
	v_lshl_add_u64 v[228:229], v[228:229], 0, s[62:63]
	s_add_i32 m0, s31, s65
	s_nop 0
	global_load_lds_dwordx4 v[228:229], off nt
	v_add_f32_e32 v80, v94, v80
	v_add_f32_e32 v80, v95, v80
	v_add_f32_e32 v80, v64, v80
	v_add_f32_e32 v80, v65, v80
	v_cvt_pk_f16_f32 v130, v92, v93
	v_cvt_pk_f16_f32 v131, v94, v95
	ds_read_b64_tr_b16 v[148:149], v138 offset:26624
	ds_read_b64_tr_b16 v[150:151], v138 offset:27136
	v_lshl_add_u64 v[192:193], v[174:175], 0, s[2:3]
	v_lshl_add_u64 v[228:229], v[192:193], 0, s[10:11]
	v_lshl_add_u64 v[228:229], v[228:229], 0, s[62:63]
	s_add_i32 m0, s34, s65
	s_nop 0
	global_load_lds_dwordx4 v[228:229], off nt
	v_add_f32_e32 v80, v66, v80
	v_add_f32_e32 v80, v67, v80
	v_add_f32_e32 v80, v68, v80
	v_add_f32_e32 v80, v69, v80
	v_cvt_pk_f16_f32 v124, v64, v65
	v_cvt_pk_f16_f32 v125, v66, v67
	ds_read_b64_tr_b16 v[144:145], v138 offset:30720
	ds_read_b64_tr_b16 v[146:147], v138 offset:31232
	v_add_f32_e32 v64, v70, v80
	v_add_f32_e32 v64, v71, v64
	v_add_f32_e32 v64, v72, v64
	v_add_f32_e32 v64, v73, v64
	v_cvt_pk_f16_f32 v126, v68, v69
	v_cvt_pk_f16_f32 v127, v70, v71
	ds_read_b64_tr_b16 v[140:141], v138 offset:27648
	ds_read_b64_tr_b16 v[142:143], v138 offset:28160
	v_add_f32_e32 v64, v74, v64
	v_add_f32_e32 v64, v75, v64
	v_add_f32_e32 v64, v76, v64
	v_add_f32_e32 v64, v77, v64
	v_cvt_pk_f16_f32 v120, v72, v73
	v_cvt_pk_f16_f32 v121, v74, v75
	ds_read_b64_tr_b16 v[136:137], v138 offset:31744
	ds_read_b64_tr_b16 v[138:139], v138 offset:32256
	v_add_f32_e32 v64, v78, v64
	v_add_f32_e32 v64, v79, v64
	v_add_f32_e32 v108, 0, v64
	v_cvt_pk_f16_f32 v122, v76, v77
	v_cvt_pk_f16_f32 v123, v78, v79
	s_nop 1
	s_nop 0
	v_add_f32_e32 v185, v185, v108
	v_max_f32_e32 v108, v49, v49
	v_max_f32_e32 v109, v48, v48
	v_max_f32_e32 v108, v109, v108
	v_max3_f32 v109, v50, v51, v33
	v_max3_f32 v108, v108, v32, v34
	v_max3_f32 v108, v108, v35, v52
	v_max3_f32 v109, v109, v54, v55
	v_max3_f32 v108, v108, v53, v36
	v_max3_f32 v109, v109, v38, v39
	v_max3_f32 v108, v108, v37, v56
	v_max3_f32 v109, v109, v58, v59
	v_add_u32_e32 v221, v222, v223
	v_max3_f32 v108, v108, v57, v40
	v_max3_f32 v109, v109, v42, v43
	ds_read_b128 v[80:83], v221
	ds_read_b128 v[64:67], v161
	ds_read_b128 v[84:87], v184
	ds_read_b128 v[68:71], v211
	ds_read_b128 v[88:91], v212
	ds_read_b128 v[72:75], v213
	ds_read_b128 v[92:95], v214
	ds_read_b128 v[76:79], v215
	v_max3_f32 v108, v108, v41, v60
	v_max3_f32 v109, v109, v62, v63
	v_max3_f32 v108, v108, v61, v44
	v_max3_f32 v109, v109, v46, v47
	v_max3_f32 v108, v108, v45, v109
	v_mov_b32_e32 v109, v108
	s_nop 1
	v_permlane32_swap_b32_e32 v108, v109
	v_max_f32_e32 v109, v109, v109
	v_max_f32_e32 v108, v108, v108
	v_max_f32_e32 v108, v108, v109
	v_fma_f32 v108, v108, s41, -v208
	v_cmp_lt_f32_e32 vcc, s29, v108
	s_cmp_lg_u64 vcc, 0
	s_cselect_b64 s[24:25], -1, 0
	s_cbranch_vccnz .LBB6_21

.LBB6_12:
	v_mfma_f32_32x32x16_f16 v[16:31], v[132:135], v[112:115], v[16:31]
	v_fma_f32 v52, v52, s41, -v208
	v_fma_f32 v53, v53, s41, -v208
	v_fma_f32 v54, v54, s41, -v208
	v_fma_f32 v55, v55, s41, -v208
	v_exp_f32_e32 v52, v52
	v_exp_f32_e32 v53, v53
	v_exp_f32_e32 v54, v54
	v_exp_f32_e32 v55, v55
	v_lshl_add_u64 v[108:109], v[182:183], 0, s[20:21]
	s_add_i32 s26, s28, s37
	s_mov_b32 m0, s26
	s_nop 0
	global_load_lds_dwordx4 v[108:109], off
	v_lshl_add_u64 v[226:227], v[108:109], 0, s[58:59]
	s_add_i32 m0, s26, 0x6800
	s_nop 0
	global_load_lds_dwordx4 v[226:227], off
	s_waitcnt lgkmcnt(0)
	v_add_u32_e32 v108, s28, v216
	v_add_u32_e32 v109, v108, v217
	v_add_u32_e32 v108, v108, v218
	ds_read_b128 v[112:115], v109
	ds_read_b128 v[116:119], v108
	v_mfma_f32_32x32x16_f16 v[0:15], v[128:131], v[104:107], v[0:15]
	v_fma_f32 v56, v56, s41, -v208
	v_fma_f32 v57, v57, s41, -v208
	v_fma_f32 v58, v58, s41, -v208
	v_fma_f32 v59, v59, s41, -v208
	v_exp_f32_e32 v56, v56
	v_exp_f32_e32 v57, v57
	v_exp_f32_e32 v58, v58
	v_exp_f32_e32 v59, v59
	ds_read_b128 v[104:107], v109 offset:2048
	ds_read_b128 v[108:111], v108 offset:2048
	v_mfma_f32_32x32x16_f16 v[16:31], v[128:131], v[152:155], v[16:31]
	v_fma_f32 v60, v60, s41, -v208
	v_fma_f32 v61, v61, s41, -v208
	v_fma_f32 v62, v62, s41, -v208
	v_fma_f32 v63, v63, s41, -v208
	v_exp_f32_e32 v60, v60
	v_exp_f32_e32 v61, v61
	v_exp_f32_e32 v62, v62
	v_exp_f32_e32 v63, v63
	v_mfma_f32_32x32x16_f16 v[0:15], v[124:127], v[148:151], v[0:15]
	v_fma_f32 v32, v32, s41, -v208
	v_fma_f32 v33, v33, s41, -v208
	v_fma_f32 v34, v34, s41, -v208
	v_fma_f32 v35, v35, s41, -v208
	v_exp_f32_e32 v32, v32
	v_exp_f32_e32 v33, v33
	v_exp_f32_e32 v34, v34
	v_exp_f32_e32 v35, v35
	s_waitcnt lgkmcnt(14)
	v_mfma_f32_32x32x16_f16 v[16:31], v[124:127], v[144:147], v[16:31]
	v_fma_f32 v36, v36, s41, -v208
	v_fma_f32 v37, v37, s41, -v208
	v_fma_f32 v38, v38, s41, -v208
	v_fma_f32 v39, v39, s41, -v208
	v_exp_f32_e32 v36, v36
	v_exp_f32_e32 v37, v37
	v_exp_f32_e32 v38, v38
	v_exp_f32_e32 v39, v39
	v_lshl_add_u64 v[194:195], v[172:173], 0, s[2:3]
	v_mfma_f32_32x32x16_f16 v[0:15], v[120:123], v[140:143], v[0:15]
	v_fma_f32 v40, v40, s41, -v208
	v_fma_f32 v41, v41, s41, -v208
	v_fma_f32 v42, v42, s41, -v208
	v_fma_f32 v43, v43, s41, -v208
	v_exp_f32_e32 v40, v40
	v_exp_f32_e32 v41, v41
	v_exp_f32_e32 v42, v42
	v_exp_f32_e32 v43, v43
	v_lshl_add_u64 v[196:197], v[170:171], 0, s[2:3]
	s_waitcnt lgkmcnt(12)
	v_mfma_f32_32x32x16_f16 v[16:31], v[120:123], v[136:139], v[16:31]
	v_fma_f32 v44, v44, s41, -v208
	v_fma_f32 v45, v45, s41, -v208
	v_fma_f32 v46, v46, s41, -v208
	v_fma_f32 v47, v47, s41, -v208
	v_exp_f32_e32 v44, v44
	v_exp_f32_e32 v45, v45
	v_exp_f32_e32 v46, v46
	v_exp_f32_e32 v47, v47
	v_lshl_add_u64 v[198:199], v[168:169], 0, s[2:3]
	v_lshl_add_u64 v[200:201], v[166:167], 0, s[2:3]
	s_waitcnt vmcnt(3) lgkmcnt(0)
	s_barrier
	s_andn2_b64 vcc, exec, s[24:25]
	s_cbranch_vccnz .LBB6_14
	ds_read_b128 v[136:139], v205 offset:49248
	ds_read_b128 v[140:143], v205 offset:49216
	ds_read_b128 v[144:147], v205 offset:49184
	ds_read_b128 v[148:151], v205 offset:49152
	s_waitcnt lgkmcnt(3)
	v_pk_mul_f32 v[14:15], v[14:15], v[138:139]
	s_waitcnt lgkmcnt(2)
	v_pk_mul_f32 v[10:11], v[10:11], v[142:143]
	s_waitcnt lgkmcnt(1)
	v_pk_mul_f32 v[6:7], v[6:7], v[146:147]
	s_waitcnt lgkmcnt(0)
	v_pk_mul_f32 v[2:3], v[2:3], v[150:151]
	v_pk_mul_f32 v[12:13], v[12:13], v[136:137]
	v_pk_mul_f32 v[8:9], v[8:9], v[140:141]
	v_pk_mul_f32 v[4:5], v[4:5], v[144:145]
	v_pk_mul_f32 v[0:1], v[0:1], v[148:149]
	v_pk_mul_f32 v[30:31], v[30:31], v[138:139]
	v_pk_mul_f32 v[26:27], v[26:27], v[142:143]
	v_pk_mul_f32 v[22:23], v[22:23], v[146:147]
	v_pk_mul_f32 v[18:19], v[18:19], v[150:151]
	v_pk_mul_f32 v[28:29], v[28:29], v[136:137]
	v_pk_mul_f32 v[24:25], v[24:25], v[140:141]
	v_pk_mul_f32 v[20:21], v[20:21], v[144:145]
	v_pk_mul_f32 v[16:17], v[16:17], v[148:149]
.LBB6_14:
	v_add_u32_e32 v138, s45, v207
	ds_read_b64_tr_b16 v[156:157], v138 offset:24576
	ds_read_b64_tr_b16 v[158:159], v138 offset:25088
	v_add_f32_e32 v120, v48, v49
	s_waitcnt lgkmcnt(4)
	v_mfma_scale_f32_32x32x64_f8f6f4 v[80:95], v[112:119], v[96:103], v[80:95], v219, v220 op_sel_hi:[0,0,0]
	v_add_f32_e32 v112, v50, v120
	v_add_f32_e32 v112, v51, v112
	v_add_f32_e32 v112, v52, v112
	v_add_f32_e32 v116, v53, v112
	v_cvt_pk_f16_f32 v132, v48, v49
	v_cvt_pk_f16_f32 v133, v50, v51
	ds_read_b64_tr_b16 v[112:113], v138 offset:28672
	ds_read_b64_tr_b16 v[114:115], v138 offset:29184
	v_add_f32_e32 v48, v54, v116
	v_add_f32_e32 v48, v55, v48
	v_add_f32_e32 v48, v56, v48
	v_add_f32_e32 v48, v57, v48
	v_cvt_pk_f16_f32 v134, v52, v53
	v_cvt_pk_f16_f32 v135, v54, v55
	s_waitcnt lgkmcnt(4)
	v_mfma_scale_f32_32x32x64_f8f6f4 v[64:79], v[104:111], v[96:103], v[64:79], v219, v220 op_sel_hi:[0,0,0]
	v_lshl_add_u64 v[228:229], v[186:187], 0, s[22:23]
	v_lshl_add_u64 v[228:229], v[228:229], 0, s[62:63]
	s_add_i32 m0, s38, s64
	s_nop 0
	global_load_lds_dwordx4 v[228:229], off nt
	ds_read_b64_tr_b16 v[104:105], v138 offset:25600
	ds_read_b64_tr_b16 v[106:107], v138 offset:26112
	v_lshl_add_u64 v[228:229], v[188:189], 0, s[22:23]
	v_lshl_add_u64 v[228:229], v[228:229], 0, s[62:63]
	s_add_i32 m0, s30, s64
	s_nop 0
	global_load_lds_dwordx4 v[228:229], off nt
	v_add_f32_e32 v48, v58, v48
	v_add_f32_e32 v48, v59, v48
	v_add_f32_e32 v48, v60, v48
	v_add_f32_e32 v48, v61, v48
	v_cvt_pk_f16_f32 v128, v56, v57
	v_cvt_pk_f16_f32 v129, v58, v59
	ds_read_b64_tr_b16 v[152:153], v138 offset:29696
	ds_read_b64_tr_b16 v[154:155], v138 offset:30208
	v_lshl_add_u64 v[228:229], v[190:191], 0, s[22:23]
	v_lshl_add_u64 v[228:229], v[228:229], 0, s[62:63]
	s_add_i32 m0, s31, s64
	s_nop 0
	global_load_lds_dwordx4 v[228:229], off nt
	v_add_f32_e32 v48, v62, v48
	v_add_f32_e32 v48, v63, v48
	v_add_f32_e32 v48, v32, v48
	v_add_f32_e32 v48, v33, v48
	v_cvt_pk_f16_f32 v130, v60, v61
	v_cvt_pk_f16_f32 v131, v62, v63
	ds_read_b64_tr_b16 v[148:149], v138 offset:26624
	ds_read_b64_tr_b16 v[150:151], v138 offset:27136
	v_lshl_add_u64 v[228:229], v[192:193], 0, s[22:23]
	v_lshl_add_u64 v[228:229], v[228:229], 0, s[62:63]
	s_add_i32 m0, s34, s64
	s_nop 0
	global_load_lds_dwordx4 v[228:229], off nt
	v_add_f32_e32 v48, v34, v48
	v_add_f32_e32 v48, v35, v48
	v_add_f32_e32 v48, v36, v48
	v_add_f32_e32 v48, v37, v48
	v_cvt_pk_f16_f32 v124, v32, v33
	v_cvt_pk_f16_f32 v125, v34, v35
	ds_read_b64_tr_b16 v[144:145], v138 offset:30720
	ds_read_b64_tr_b16 v[146:147], v138 offset:31232
	v_add_f32_e32 v32, v38, v48
	v_add_f32_e32 v32, v39, v32
	v_add_f32_e32 v32, v40, v32
	v_add_f32_e32 v32, v41, v32
	v_cvt_pk_f16_f32 v126, v36, v37
	v_cvt_pk_f16_f32 v127, v38, v39
	ds_read_b64_tr_b16 v[140:141], v138 offset:27648
	ds_read_b64_tr_b16 v[142:143], v138 offset:28160
	v_add_f32_e32 v32, v42, v32
	v_add_f32_e32 v32, v43, v32
	v_add_f32_e32 v32, v44, v32
	v_add_f32_e32 v32, v45, v32
	v_cvt_pk_f16_f32 v120, v40, v41
	v_cvt_pk_f16_f32 v121, v42, v43
	ds_read_b64_tr_b16 v[136:137], v138 offset:31744
	ds_read_b64_tr_b16 v[138:139], v138 offset:32256
	v_add_f32_e32 v32, v46, v32
	v_add_f32_e32 v32, v47, v32
	v_add_f32_e32 v108, 0, v32
	v_cvt_pk_f16_f32 v122, v44, v45
	v_cvt_pk_f16_f32 v123, v46, v47
	s_nop 1
	s_nop 0
	v_add_f32_e32 v185, v185, v108
	v_max_f32_e32 v108, v81, v81
	v_max_f32_e32 v109, v80, v80
	v_max_f32_e32 v108, v109, v108
	v_max3_f32 v109, v82, v83, v65
	v_max3_f32 v108, v108, v64, v66
	v_max3_f32 v108, v108, v67, v84
	v_max3_f32 v109, v109, v86, v87
	v_max3_f32 v108, v108, v85, v68
	v_max3_f32 v109, v109, v70, v71
	v_max3_f32 v108, v108, v69, v88
	v_max3_f32 v109, v109, v90, v91
	v_max3_f32 v108, v108, v89, v72
	v_max3_f32 v109, v109, v74, v75
	ds_read_b128 v[48:51], v221 offset:32768
	ds_read_b128 v[32:35], v161 offset:32768
	ds_read_b128 v[52:55], v184 offset:32768
	ds_read_b128 v[36:39], v211 offset:32768
	ds_read_b128 v[56:59], v212 offset:32768
	ds_read_b128 v[40:43], v213 offset:32768
	ds_read_b128 v[60:63], v214 offset:32768
	ds_read_b128 v[44:47], v215 offset:32768
	v_max3_f32 v108, v108, v73, v92
	v_max3_f32 v109, v109, v94, v95
	v_max3_f32 v108, v108, v93, v76
	v_max3_f32 v109, v109, v78, v79
	v_max3_f32 v108, v108, v77, v109
	v_mov_b32_e32 v109, v108
	s_nop 1
	v_permlane32_swap_b32_e32 v108, v109
	v_max_f32_e32 v109, v109, v109
	v_max_f32_e32 v108, v108, v108
	v_max_f32_e32 v108, v108, v109
	v_fma_f32 v108, v108, s41, -v208
	v_cmp_lt_f32_e32 vcc, s29, v108
	s_cmp_lg_u64 vcc, 0
	s_cselect_b64 s[24:25], -1, 0
	s_cbranch_vccnz .LBB6_24

.LBB6_17:
	s_add_i32 s26, s28, 0x2000
	s_cmpk_lg_i32 s28, 0x4000
	s_cselect_b32 s45, s26, 0
	v_mfma_f32_32x32x16_f16 v[16:31], v[132:135], v[112:115], v[16:31]
	v_fma_f32 v84, v84, s41, -v208
	v_fma_f32 v85, v85, s41, -v208
	v_fma_f32 v86, v86, s41, -v208
	v_fma_f32 v87, v87, s41, -v208
	v_exp_f32_e32 v84, v84
	v_exp_f32_e32 v85, v85
	v_exp_f32_e32 v86, v86
	v_exp_f32_e32 v87, v87
	v_lshl_add_u64 v[182:183], v[182:183], 0, s[12:13]
	s_add_i32 s26, s45, s37
	s_mov_b32 m0, s26
	s_nop 0
	global_load_lds_dwordx4 v[182:183], off
	v_lshl_add_u64 v[226:227], v[182:183], 0, s[58:59]
	s_add_i32 m0, s26, 0x6800
	s_nop 0
	global_load_lds_dwordx4 v[226:227], off
	s_waitcnt lgkmcnt(0)
	v_add_u32_e32 v108, s45, v216
	v_add_u32_e32 v109, v108, v217
	v_add_u32_e32 v108, v108, v218
	ds_read_b128 v[112:115], v109
	ds_read_b128 v[116:119], v108
	v_mfma_f32_32x32x16_f16 v[0:15], v[128:131], v[104:107], v[0:15]
	v_fma_f32 v88, v88, s41, -v208
	v_fma_f32 v89, v89, s41, -v208
	v_fma_f32 v90, v90, s41, -v208
	v_fma_f32 v91, v91, s41, -v208
	v_exp_f32_e32 v88, v88
	v_exp_f32_e32 v89, v89
	v_exp_f32_e32 v90, v90
	v_exp_f32_e32 v91, v91
	ds_read_b128 v[104:107], v109 offset:2048
	ds_read_b128 v[108:111], v108 offset:2048
	v_mfma_f32_32x32x16_f16 v[16:31], v[128:131], v[152:155], v[16:31]
	v_fma_f32 v92, v92, s41, -v208
	v_fma_f32 v93, v93, s41, -v208
	v_fma_f32 v94, v94, s41, -v208
	v_fma_f32 v95, v95, s41, -v208
	v_exp_f32_e32 v92, v92
	v_exp_f32_e32 v93, v93
	v_exp_f32_e32 v94, v94
	v_exp_f32_e32 v95, v95
	v_mfma_f32_32x32x16_f16 v[0:15], v[124:127], v[148:151], v[0:15]
	v_fma_f32 v64, v64, s41, -v208
	v_fma_f32 v65, v65, s41, -v208
	v_fma_f32 v66, v66, s41, -v208
	v_fma_f32 v67, v67, s41, -v208
	v_exp_f32_e32 v64, v64
	v_exp_f32_e32 v65, v65
	v_exp_f32_e32 v66, v66
	v_exp_f32_e32 v67, v67
	s_waitcnt lgkmcnt(14)
	v_mfma_f32_32x32x16_f16 v[16:31], v[124:127], v[144:147], v[16:31]
	v_fma_f32 v68, v68, s41, -v208
	v_fma_f32 v69, v69, s41, -v208
	v_fma_f32 v70, v70, s41, -v208
	v_fma_f32 v71, v71, s41, -v208
	v_exp_f32_e32 v68, v68
	v_exp_f32_e32 v69, v69
	v_exp_f32_e32 v70, v70
	v_exp_f32_e32 v71, v71
	v_mfma_f32_32x32x16_f16 v[0:15], v[120:123], v[140:143], v[0:15]
	v_fma_f32 v72, v72, s41, -v208
	v_fma_f32 v73, v73, s41, -v208
	v_fma_f32 v74, v74, s41, -v208
	v_fma_f32 v75, v75, s41, -v208
	v_exp_f32_e32 v72, v72
	v_exp_f32_e32 v73, v73
	v_exp_f32_e32 v74, v74
	v_exp_f32_e32 v75, v75
	s_waitcnt lgkmcnt(12)
	v_mfma_f32_32x32x16_f16 v[16:31], v[120:123], v[136:139], v[16:31]
	v_fma_f32 v76, v76, s41, -v208
	v_fma_f32 v77, v77, s41, -v208
	v_fma_f32 v78, v78, s41, -v208
	v_fma_f32 v79, v79, s41, -v208
	v_exp_f32_e32 v76, v76
	v_exp_f32_e32 v77, v77
	v_exp_f32_e32 v78, v78
	v_exp_f32_e32 v79, v79
	s_waitcnt vmcnt(3) lgkmcnt(0)
	s_barrier
	s_andn2_b64 vcc, exec, s[24:25]
	s_cbranch_vccnz .LBB6_19
	ds_read_b128 v[136:139], v205 offset:49248
	ds_read_b128 v[140:143], v205 offset:49216
	ds_read_b128 v[144:147], v205 offset:49184
	ds_read_b128 v[148:151], v205 offset:49152
	s_waitcnt lgkmcnt(3)
	v_pk_mul_f32 v[14:15], v[14:15], v[138:139]
	s_waitcnt lgkmcnt(2)
	v_pk_mul_f32 v[10:11], v[10:11], v[142:143]
	s_waitcnt lgkmcnt(1)
	v_pk_mul_f32 v[6:7], v[6:7], v[146:147]
	s_waitcnt lgkmcnt(0)
	v_pk_mul_f32 v[2:3], v[2:3], v[150:151]
	v_pk_mul_f32 v[12:13], v[12:13], v[136:137]
	v_pk_mul_f32 v[8:9], v[8:9], v[140:141]
	v_pk_mul_f32 v[4:5], v[4:5], v[144:145]
	v_pk_mul_f32 v[0:1], v[0:1], v[148:149]
	v_pk_mul_f32 v[30:31], v[30:31], v[138:139]
	v_pk_mul_f32 v[26:27], v[26:27], v[142:143]
	v_pk_mul_f32 v[22:23], v[22:23], v[146:147]
	v_pk_mul_f32 v[18:19], v[18:19], v[150:151]
	v_pk_mul_f32 v[28:29], v[28:29], v[136:137]
	v_pk_mul_f32 v[24:25], v[24:25], v[140:141]
	v_pk_mul_f32 v[20:21], v[20:21], v[144:145]
	v_pk_mul_f32 v[16:17], v[16:17], v[148:149]

.LBB6_27:
	ds_read_b64_tr_b16 v[156:157], v207 offset:32768
	ds_read_b64_tr_b16 v[158:159], v207 offset:33280
	v_add_f32_e32 v120, v80, v81
	v_mov_b32_e32 v121, 0x7f7f7f7f
	v_mov_b32_e32 v124, 0x7c7c7c7c
	s_waitcnt lgkmcnt(4)
	v_mfma_scale_f32_32x32x64_f8f6f4 v[48:63], v[112:119], v[96:103], v[48:63], v121, v124 op_sel_hi:[0,0,0]
	v_add_f32_e32 v112, v82, v120
	v_add_f32_e32 v112, v83, v112
	v_add_f32_e32 v112, v84, v112
	v_add_f32_e32 v116, v85, v112
	v_cvt_pk_f16_f32 v132, v80, v81
	v_cvt_pk_f16_f32 v133, v82, v83
	ds_read_b64_tr_b16 v[112:113], v207 offset:36864
	ds_read_b64_tr_b16 v[114:115], v207 offset:37376
	v_add_f32_e32 v80, v86, v116
	v_add_f32_e32 v80, v87, v80
	v_add_f32_e32 v80, v88, v80
	v_add_f32_e32 v80, v89, v80
	v_cvt_pk_f16_f32 v134, v84, v85
	v_cvt_pk_f16_f32 v135, v86, v87
	s_waitcnt lgkmcnt(4)
	v_mfma_scale_f32_32x32x64_f8f6f4 v[32:47], v[104:111], v[96:103], v[32:47], v121, v124 op_sel_hi:[0,0,0]
	ds_read_b64_tr_b16 v[104:105], v207 offset:33792
	ds_read_b64_tr_b16 v[106:107], v207 offset:34304
	v_add_f32_e32 v80, v90, v80
	v_add_f32_e32 v80, v91, v80
	v_add_f32_e32 v80, v92, v80
	v_add_f32_e32 v80, v93, v80
	v_cvt_pk_f16_f32 v128, v88, v89
	v_cvt_pk_f16_f32 v129, v90, v91
	ds_read_b64_tr_b16 v[152:153], v207 offset:37888
	ds_read_b64_tr_b16 v[154:155], v207 offset:38400
	v_add_f32_e32 v80, v94, v80
	v_add_f32_e32 v80, v95, v80
	v_add_f32_e32 v80, v64, v80
	v_add_f32_e32 v80, v65, v80
	v_cvt_pk_f16_f32 v130, v92, v93
	v_cvt_pk_f16_f32 v131, v94, v95
	ds_read_b64_tr_b16 v[148:149], v207 offset:34816
	ds_read_b64_tr_b16 v[150:151], v207 offset:35328
	v_add_f32_e32 v80, v66, v80
	v_add_f32_e32 v80, v67, v80
	v_add_f32_e32 v80, v68, v80
	v_add_f32_e32 v80, v69, v80
	v_cvt_pk_f16_f32 v124, v64, v65
	v_cvt_pk_f16_f32 v125, v66, v67
	ds_read_b64_tr_b16 v[144:145], v207 offset:38912
	ds_read_b64_tr_b16 v[146:147], v207 offset:39424
	v_add_f32_e32 v64, v70, v80
	v_add_f32_e32 v64, v71, v64
	v_add_f32_e32 v64, v72, v64
	v_add_f32_e32 v64, v73, v64
	v_cvt_pk_f16_f32 v126, v68, v69
	v_cvt_pk_f16_f32 v127, v70, v71
	ds_read_b64_tr_b16 v[140:141], v207 offset:35840
	ds_read_b64_tr_b16 v[142:143], v207 offset:36352
	v_add_f32_e32 v64, v74, v64
	v_add_f32_e32 v64, v75, v64
	v_add_f32_e32 v64, v76, v64
	v_add_f32_e32 v64, v77, v64
	v_cvt_pk_f16_f32 v120, v72, v73
	v_cvt_pk_f16_f32 v121, v74, v75
	ds_read_b64_tr_b16 v[136:137], v207 offset:39936
	ds_read_b64_tr_b16 v[138:139], v207 offset:40448
	v_add_f32_e32 v64, v78, v64
	v_add_f32_e32 v64, v79, v64
	v_add_f32_e32 v108, 0, v64
	v_cvt_pk_f16_f32 v122, v76, v77
	v_cvt_pk_f16_f32 v123, v78, v79
	s_nop 1
	s_nop 0
	v_add_f32_e32 v180, v185, v108
	v_max_f32_e32 v108, v49, v49
	v_max_f32_e32 v109, v48, v48
	v_max_f32_e32 v108, v109, v108
	v_max3_f32 v109, v50, v51, v33
	v_max3_f32 v108, v108, v32, v34
	v_max3_f32 v108, v108, v35, v52
	v_max3_f32 v109, v109, v54, v55
	v_max3_f32 v108, v108, v53, v36
	v_max3_f32 v109, v109, v38, v39
	v_max3_f32 v108, v108, v37, v56
	v_max3_f32 v109, v109, v58, v59
	v_max3_f32 v108, v108, v57, v40
	v_max3_f32 v109, v109, v42, v43
	ds_read_b128 v[80:83], v221
	ds_read_b128 v[64:67], v161
	ds_read_b128 v[84:87], v184
	ds_read_b128 v[68:71], v211
	ds_read_b128 v[88:91], v212
	ds_read_b128 v[72:75], v213
	ds_read_b128 v[92:95], v214
	ds_read_b128 v[76:79], v215
	v_max3_f32 v108, v108, v41, v60
	v_max3_f32 v109, v109, v62, v63
	v_max3_f32 v108, v108, v61, v44
	v_max3_f32 v109, v109, v46, v47
	v_max3_f32 v108, v108, v45, v109
	v_mov_b32_e32 v109, v108
	s_nop 1
	v_permlane32_swap_b32_e32 v108, v109
	v_max_f32_e32 v109, v109, v109
	v_max_f32_e32 v108, v108, v108
	v_max_f32_e32 v108, v108, v109
	s_mov_b32 s8, 0x3fb8aa3b
	v_fma_f32 v108, v108, s8, -v208
	s_mov_b32 s2, 0x41000000
	v_cmp_lt_f32_e32 vcc, s2, v108
	s_cmp_lg_u64 vcc, 0
	s_cselect_b64 s[2:3], -1, 0
	s_cbranch_vccnz .LBB6_39
